# mixer: chunk-end wait covers only the next chunk's q/k rows; v rows waited where first read
# speedup vs baseline: 1.0090x; 1.0032x over previous
.LBB0_465:
	s_waitcnt lgkmcnt(0)
	s_barrier
	ds_read_b128 v[10:13], v127
	ds_read_b128 v[14:17], v127 offset:64
	ds_read_b128 v[56:59], v127 offset:128
	ds_read_b128 v[60:63], v127 offset:192
	ds_read_b128 v[64:67], v128 offset:17408
	ds_read_b128 v[68:71], v128 offset:17472
	ds_read_b128 v[72:75], v128 offset:17536
	ds_read_b128 v[76:79], v128 offset:17600
	ds_read_b128 v[176:179], v128 offset:21760
	ds_read_b128 v[180:183], v128 offset:21824
	ds_read_b128 v[184:187], v128 offset:21888
	ds_read_b128 v[188:191], v128 offset:21952
	s_waitcnt lgkmcnt(7)
	v_mfma_f32_16x16x32_bf16 v[2:5], v[64:67], v[10:13], 0
	s_waitcnt lgkmcnt(6)
	v_mfma_f32_16x16x32_bf16 v[2:5], v[68:71], v[14:17], v[2:5]
	s_waitcnt lgkmcnt(3)
	v_mfma_f32_16x16x32_bf16 v[6:9], v[176:179], v[10:13], 0
	v_mfma_f32_16x16x32_bf16 v[2:5], v[72:75], v[56:59], v[2:5]
	s_waitcnt lgkmcnt(2)
	v_mfma_f32_16x16x32_bf16 v[6:9], v[180:183], v[14:17], v[6:9]
	v_mfma_f32_16x16x32_bf16 v[2:5], v[76:79], v[60:63], v[2:5]
	s_waitcnt lgkmcnt(1)
	v_mfma_f32_16x16x32_bf16 v[6:9], v[184:187], v[56:59], v[6:9]
	s_waitcnt lgkmcnt(0)
	v_mfma_f32_16x16x32_bf16 v[6:9], v[188:191], v[60:63], v[6:9]
	s_nop 6
	v_cndmask_b32_e64 v56, v2, 0, s[44:45]
	v_cndmask_b32_e64 v57, 0, v3, s[46:47]
	v_cndmask_b32_e64 v58, v4, 0, s[48:49]
	v_cndmask_b32_e64 v59, v5, 0, s[50:51]
	v_cvt_pk_bf16_f32 v56, v56, v57
	v_cvt_pk_bf16_f32 v57, v58, v59
	ds_write_b64 v129, v[56:57]
	v_cndmask_b32_e64 v6, v6, 0, s[52:53]
	v_cndmask_b32_e64 v7, 0, v7, s[54:55]
	v_cndmask_b32_e64 v8, v8, 0, s[56:57]
	v_cndmask_b32_e64 v9, v9, 0, s[58:59]
	v_cvt_pk_bf16_f32 v6, v6, v7
	v_cvt_pk_bf16_f32 v7, v8, v9
	ds_write_b64 v130, v[6:7]
	s_waitcnt lgkmcnt(0)
	s_barrier
	ds_read_b128 v[10:13], v131
	ds_read_b128 v[14:17], v132
	ds_read_b128 v[56:59], v133
	ds_read_b128 v[60:63], v131 offset:64
	ds_read_b128 v[64:67], v132 offset:64
	ds_read_b128 v[68:71], v133 offset:64
	ds_read_b128 v[72:75], v138
	ds_read_b128 v[76:79], v134 offset:52224
	ds_read_b128 v[176:179], v137
	ds_read_b128 v[180:183], v137 offset:2304
	ds_read_b128 v[184:187], v137 offset:4608
	ds_read_b128 v[188:191], v137 offset:6912
	ds_read_b128 v[200:203], v134 offset:52288
	ds_read_b128 v[204:207], v137 offset:64
	ds_read_b128 v[208:211], v137 offset:2368
	s_waitcnt lgkmcnt(13)
	v_mfma_f32_16x16x32_bf16 v[6:9], v[10:13], v[14:17], 0
	s_waitcnt lgkmcnt(12)
	v_mfma_f32_16x16x32_bf16 v[2:5], v[10:13], v[56:59], 0
	ds_read_b128 v[212:215], v137 offset:4672
	ds_read_b128 v[220:223], v137 offset:6976
	ds_read_b128 v[224:227], v135
	s_waitcnt lgkmcnt(13)
	v_mfma_f32_16x16x32_bf16 v[6:9], v[60:63], v[64:67], v[6:9]
	s_waitcnt lgkmcnt(12)
	v_mfma_f32_16x16x32_bf16 v[2:5], v[60:63], v[68:71], v[2:5]
	ds_read_b128 v[232:235], v128
	ds_read_b128 v[236:239], v136
	ds_read_b128 v[14:17], v135 offset:64
	s_waitcnt lgkmcnt(14)
	v_pk_mul_f32 v[22:23], v[22:23], v[72:73]
	v_pk_mul_f32 v[24:25], v[24:25], v[74:75]
	v_pk_mul_f32 v[26:27], v[26:27], v[72:73]
	v_pk_mul_f32 v[28:29], v[28:29], v[74:75]
	v_pk_mul_f32 v[30:31], v[30:31], v[72:73]
	v_pk_mul_f32 v[32:33], v[32:33], v[74:75]
	v_pk_mul_f32 v[34:35], v[34:35], v[72:73]
	v_pk_mul_f32 v[36:37], v[36:37], v[74:75]
	s_waitcnt lgkmcnt(12)
	v_mfma_f32_16x16x32_bf16 v[22:25], v[76:79], v[176:179], v[22:25]
	s_waitcnt lgkmcnt(11)
	v_mfma_f32_16x16x32_bf16 v[26:29], v[76:79], v[180:183], v[26:29]
	s_waitcnt lgkmcnt(10)
	v_mfma_f32_16x16x32_bf16 v[30:33], v[76:79], v[184:187], v[30:33]
	s_waitcnt lgkmcnt(9)
	v_mfma_f32_16x16x32_bf16 v[34:37], v[76:79], v[188:191], v[34:37]
	ds_read_b128 v[10:13], v128 offset:64
	ds_read_b128 v[56:59], v136 offset:64
	ds_read_b128 v[64:67], v135 offset:128
	ds_read_b128 v[60:63], v128 offset:128
	s_waitcnt lgkmcnt(11)
	v_mfma_f32_16x16x32_bf16 v[22:25], v[200:203], v[204:207], v[22:25]
	s_waitcnt lgkmcnt(10)
	v_mfma_f32_16x16x32_bf16 v[26:29], v[200:203], v[208:211], v[26:29]
	ds_read_b128 v[68:71], v136 offset:128
	ds_read_b128 v[72:75], v135 offset:192
	s_waitcnt lgkmcnt(11)
	v_mfma_f32_16x16x32_bf16 v[30:33], v[200:203], v[212:215], v[30:33]
	s_waitcnt lgkmcnt(10)
	v_mfma_f32_16x16x32_bf16 v[34:37], v[200:203], v[220:223], v[34:37]
	ds_read_b128 v[176:179], v128 offset:192
	ds_read_b128 v[180:183], v136 offset:192
	s_waitcnt lgkmcnt(10)
	v_mfma_f32_16x16x32_bf16 v[6:9], v[224:227], v[232:235], v[6:9]
	s_waitcnt lgkmcnt(9)
	v_mfma_f32_16x16x32_bf16 v[2:5], v[224:227], v[236:239], v[2:5]
	s_waitcnt lgkmcnt(7)
	v_mfma_f32_16x16x32_bf16 v[6:9], v[14:17], v[10:13], v[6:9]
	s_waitcnt lgkmcnt(6)
	v_mfma_f32_16x16x32_bf16 v[2:5], v[14:17], v[56:59], v[2:5]
	s_waitcnt lgkmcnt(4)
	v_mfma_f32_16x16x32_bf16 v[6:9], v[64:67], v[60:63], v[6:9]
	s_waitcnt lgkmcnt(3)
	v_mfma_f32_16x16x32_bf16 v[2:5], v[64:67], v[68:71], v[2:5]
	s_waitcnt lgkmcnt(1)
	v_mfma_f32_16x16x32_bf16 v[6:9], v[72:75], v[176:179], v[6:9]
	s_waitcnt lgkmcnt(0)
	v_mfma_f32_16x16x32_bf16 v[2:5], v[72:75], v[180:183], v[2:5]
	v_add_u32_e32 v57, s24, v118
	v_add_u32_e32 v56, s4, v109
	v_add_u32_e32 v58, 0x7ff, v57
	s_add_i32 s4, s4, 64
	s_sub_i32 s24, s24, 64
	v_cndmask_b32_e64 v58, v58, v56, s[76:77]
	s_cmpk_eq_i32 s4, 0x800
	s_waitcnt vmcnt(1)
	s_nop 0
	v_cvt_pk_bf16_f32 v6, v6, v7
	v_cvt_pk_bf16_f32 v7, v8, v9
	v_or_b32_e32 v8, s84, v58
	v_ashrrev_i32_e32 v9, 31, v8
	v_lshl_add_u64 v[8:9], v[8:9], 0, s[2:3]
	v_mad_u64_u32 v[14:15], s[8:9], v8, s11, v[54:55]
	v_mad_i32_i24 v15, v9, s11, v15
	global_store_dwordx2 v[14:15], v[6:7], off
	v_add_u32_e32 v6, 16, v56
	v_add_u32_e32 v7, 0x7ef, v57
	v_cndmask_b32_e64 v6, v7, v6, s[76:77]
	v_cvt_pk_bf16_f32 v2, v2, v3
	v_cvt_pk_bf16_f32 v3, v4, v5
	v_or_b32_e32 v4, s84, v6
	v_ashrrev_i32_e32 v5, 31, v4
	v_lshl_add_u64 v[4:5], v[4:5], 0, s[2:3]
	v_mad_u64_u32 v[6:7], s[8:9], v4, s11, v[54:55]
	v_mad_i32_i24 v7, v5, s11, v7
	global_store_dwordx2 v[6:7], v[2:3], off
	s_cbranch_scc1 .LBB0_448

.LBB0_470:
	s_cmpk_eq_i32 s4, 0x7c0
	s_cbranch_scc1 .Lmx_vw_last
	s_waitcnt vmcnt(6)
	s_branch .Lmx_vw_done
.Lmx_vw_last:
	s_waitcnt vmcnt(2)
